# baseline (speedup 1.0000x reference)
_Z10attn64_fwdPKDF16_S0_S0_PDF16_:
	s_bfe_u32 s3, s2, 0x40003
	s_lshl_b32 s27, s3, 1
	v_readfirstlane_b32 s19, v0
	s_mov_b32 s55, 0
	s_mov_b32 s57, 0
	s_xor_b32 s28, s27, 31
	s_cmpk_lt_u32 s19, 0x100
	s_cselect_b64 s[4:5], -1, 0
	s_and_b64 s[4:5], s[4:5], exec
	s_cselect_b32 s29, s28, 0x63
	s_sub_i32 s8, 34, s27
	v_sub_co_u32_e64 v1, s[4:5], 3, s29
	s_and_b64 s[4:5], s[4:5], exec
	v_readfirstlane_b32 s4, v1
	s_cselect_b32 s9, 3, s4
	s_cmpk_lt_u32 s19, 0x100
	s_cselect_b64 s[4:5], -1, 0
	s_and_b64 s[4:5], s[4:5], exec
	v_sub_co_u32_e64 v1, s[6:7], 2, s29
	s_cselect_b32 s18, s9, s8
	s_sub_i32 s8, 33, s27
	s_and_b64 s[4:5], s[6:7], exec
	v_readfirstlane_b32 s4, v1
	s_cselect_b32 s6, 2, s4
	s_cmpk_lt_u32 s19, 0x100
	s_cselect_b64 s[4:5], -1, 0
	s_and_b64 s[4:5], s[4:5], exec
	s_cselect_b32 s24, s6, s8
	s_sub_i32 s4, 32, s27
	s_cmp_lg_u32 s29, 1
	s_cselect_b64 s[6:7], -1, 0
	s_cmpk_lt_u32 s19, 0x100
	v_cndmask_b32_e64 v2, 0, 1, s[6:7]
	s_cselect_b64 s[6:7], -1, 0
	s_load_dwordx8 s[8:15], s[0:1], 0x0
	s_mul_i32 s16, s28, 0x11000
	s_and_b64 s[0:1], s[6:7], exec
	s_cselect_b32 s23, 0, s16
	s_lshr_b32 s1, s2, 4
	s_and_b32 s0, s2, 7
	s_and_b32 s1, s1, 0x3fffff8
	s_or_b32 s2, s1, s0
	s_lshr_b32 s0, s19, 8
	v_mov_b32_e32 v3, s4
	s_mul_i32 s1, s0, 0xc000
	s_bfe_u32 s0, s19, 0x20006
	s_lshl_b32 s4, s2, 6
	s_lshr_b32 s2, s19, 4
	s_mov_b32 s5, 0
	v_cndmask_b32_e64 v6, v3, v2, s[6:7]
	s_lshl_b32 s3, s3, 7
	s_lshl_b32 s16, s0, 5
	v_and_b32_e32 v3, 7, v0
	s_and_b32 s2, s2, 4
	v_bfe_u32 v4, v0, 4, 2
	s_or_b32 s17, s16, s3
	s_add_i32 s22, s1, 0
	s_and_b32 s1, s19, 0x3fffffc0
	v_bitop3_b32 v4, s2, v3, v4 bitop3:0x36
	s_lshl_b64 s[2:3], s[4:5], 1
	s_waitcnt lgkmcnt(0)
	s_add_u32 s20, s12, s2
	s_addc_u32 s21, s13, s3
	s_lshl_b32 s4, s0, 10
	s_add_i32 s30, s4, s22
	v_bfe_u32 v226, v0, 3, 3
	s_cmpk_gt_u32 s19, 0xff
	v_lshl_or_b32 v2, s0, 3, v226
	s_cselect_b64 s[12:13], -1, 0
	s_xor_b32 s25, s17, 0xf80
	v_mul_u32_u24_e32 v2, 0x440, v2
	s_add_u32 s10, s10, s2
	v_lshlrev_b32_e32 v35, 1, v0
	v_lshlrev_b32_e32 v227, 3, v3
	s_addc_u32 s11, s11, s3
	v_lshlrev_b32_e32 v126, 1, v2
	v_mov_b32_e32 v127, 0
	v_bitop3_b32 v7, v35, v227, 32 bitop3:0x6c
	v_lshl_add_u64 v[2:3], s[10:11], 0, v[126:127]
	v_lshlrev_b32_e32 v4, 4, v4
	v_mov_b32_e32 v5, v127
	v_lshl_add_u64 v[222:223], v[2:3], 0, v[4:5]
	v_lshl_add_u64 v[2:3], s[20:21], 0, v[126:127]
	v_lshlrev_b32_e32 v126, 1, v7
	s_lshl_b32 s4, s23, 1
	v_lshl_add_u64 v[224:225], v[2:3], 0, v[126:127]
	v_lshl_add_u64 v[2:3], v[222:223], 0, s[4:5]
	s_mov_b32 m0, s30
	s_nop 0
	global_load_lds_dwordx4 v[2:3], off
	s_mov_b64 s[10:11], 0x11000
	v_lshl_add_u64 v[2:3], v[2:3], 0, s[10:11]
	s_add_i32 s19, s30, 0x1000
	s_mov_b32 m0, s19
	s_nop 0
	global_load_lds_dwordx4 v[2:3], off
	s_add_i32 s31, s30, 0x6000
	v_lshl_add_u64 v[2:3], v[224:225], 0, s[4:5]
	s_mov_b32 m0, s31
	s_nop 0
	global_load_lds_dwordx4 v[2:3], off
	s_add_i32 s4, s31, 0x1000
	v_lshl_add_u64 v[2:3], v[2:3], 0, s[10:11]
	s_mov_b32 m0, s4
	s_nop 0
	global_load_lds_dwordx4 v[2:3], off
	s_mov_b32 s4, 0x22000
	v_mul_lo_u32 v126, v6, s4
	s_add_i32 s4, s30, 0x2000
	v_lshl_add_u64 v[2:3], v[222:223], 0, v[126:127]
	s_mov_b32 m0, s4
	s_nop 0
	global_load_lds_dwordx4 v[2:3], off
	s_add_i32 s4, s30, 0x3000
	s_mul_i32 s23, s25, 0x440
	v_lshl_add_u64 v[2:3], v[2:3], 0, s[10:11]
	s_mov_b32 m0, s4
	s_nop 0
	global_load_lds_dwordx4 v[2:3], off
	s_lshl_b32 s4, s23, 1
	s_add_u32 s4, s8, s4
	v_and_b32_e32 v228, 31, v0
	v_bfe_u32 v1, v0, 5, 1
	s_addc_u32 s21, s9, 0
	s_add_u32 s20, s4, s2
	v_mul_u32_u24_e32 v2, 0x440, v228
	v_lshlrev_b32_e32 v233, 4, v1
	s_addc_u32 s21, s21, s3
	v_lshl_or_b32 v34, v2, 1, v233
	global_load_dwordx4 v[146:149], v34, s[20:21]
	global_load_dwordx4 v[150:153], v34, s[20:21] offset:32
	global_load_dwordx4 v[154:157], v34, s[20:21] offset:64
	global_load_dwordx4 v[158:161], v34, s[20:21] offset:96
	v_lshrrev_b32_e32 v2, 1, v0
	v_lshl_add_u32 v44, v228, 7, s22
	v_bitop3_b32 v2, v1, v2, 7 bitop3:0x78
	s_mul_i32 s20, s24, 0x11000
	v_lshl_add_u32 v234, v2, 4, v44
	v_mov_b32_e32 v2, v127
	v_mov_b32_e32 v3, v127
	v_mov_b32_e32 v4, v127
	v_mov_b32_e32 v6, v127
	v_mov_b32_e32 v7, v127
	v_mov_b32_e32 v8, v127
	v_mov_b32_e32 v9, v127
	v_mov_b32_e32 v10, v127
	v_mov_b32_e32 v11, v127
	v_mov_b32_e32 v12, v127
	v_mov_b32_e32 v13, v127
	v_mov_b32_e32 v14, v127
	v_mov_b32_e32 v15, v127
	v_mov_b32_e32 v16, v127
	v_mov_b32_e32 v17, v127
	s_ashr_i32 s21, s20, 31
	v_lshl_add_u64 v[18:19], s[20:21], 1, v[222:223]
	s_add_i32 s4, s30, 0x4000
	s_mov_b32 m0, s4
	s_nop 0
	global_load_lds_dwordx4 v[18:19], off
	v_lshl_add_u64 v[18:19], v[18:19], 0, s[10:11]
	s_add_i32 s4, s30, 0x5000
	s_mov_b32 m0, s4
	s_nop 0
	global_load_lds_dwordx4 v[18:19], off
	s_waitcnt vmcnt(6) lgkmcnt(0)
	s_barrier
	ds_read_b128 v[36:39], v234
	ds_read_b128 v[40:43], v234 offset:4096
	s_waitcnt vmcnt(3) lgkmcnt(1)
	v_mfma_f32_32x32x16_f16 v[18:33], v[36:39], v[146:149], v[2:17]
	v_bfe_u32 v45, v0, 1, 3
	v_bitop3_b32 v36, v1, v45, 2 bitop3:0x36
	v_lshl_add_u32 v235, v36, 4, v44
	v_lshlrev_b32_e32 v229, 9, v1
	s_mul_i32 s20, s18, 0x11000
	s_ashr_i32 s21, s20, 31
	s_lshl_b32 s1, s1, 2
	s_waitcnt lgkmcnt(0)
	v_mfma_f32_32x32x16_f16 v[2:17], v[40:43], v[146:149], v[2:17]
	ds_read_b128 v[36:39], v235
	ds_read_b128 v[40:43], v235 offset:4096
	s_add_i32 s24, s1, 0
	s_lshl_b32 s25, s0, 11
	s_lshl_b32 s1, s0, 13
	s_lshl_b32 s0, s0, 8
	s_add_i32 s1, s1, 0
	s_add_i32 s0, s0, 0
	s_waitcnt vmcnt(2) lgkmcnt(1)
	v_mfma_f32_32x32x16_f16 v[18:33], v[36:39], v[150:153], v[18:33]
	v_bitop3_b32 v36, v1, v45, 4 bitop3:0x36
	v_lshl_add_u32 v236, v36, 4, v44
	s_add_i32 s24, s24, 0x18000
	s_mul_i32 s26, s17, 0x440
	v_lshlrev_b32_e32 v230, 2, v1
	s_mov_b32 s38, 1
	s_movk_i32 s35, 0x2000
	s_waitcnt lgkmcnt(0)
	v_mfma_f32_32x32x16_f16 v[2:17], v[40:43], v[150:153], v[2:17]
	ds_read_b128 v[36:39], v236
	ds_read_b128 v[40:43], v236 offset:4096
	s_movk_i32 s36, 0x4000
	s_mov_b32 s34, 0x41000000
	v_or_b32_e32 v241, s16, v228
	v_or_b32_e32 v242, 0xfffff840, v230
	v_or_b32_e32 v243, 0xfffff880, v230
	v_mov_b32_e32 v244, 0x22000
	s_waitcnt vmcnt(1) lgkmcnt(1)
	v_mfma_f32_32x32x16_f16 v[18:33], v[36:39], v[154:157], v[18:33]
	v_bitop3_b32 v36, v1, v45, 6 bitop3:0x36
	v_lshl_add_u32 v237, v36, 4, v44
	v_mov_b32_e32 v245, 0xff800000
	v_mov_b32_e32 v246, v127
	v_mov_b32_e32 v247, v127
	s_waitcnt lgkmcnt(0)
	v_mfma_f32_32x32x16_f16 v[2:17], v[40:43], v[154:157], v[2:17]
	ds_read_b128 v[36:39], v237
	ds_read_b128 v[40:43], v237 offset:4096
	s_waitcnt vmcnt(0) lgkmcnt(1)
	v_mfma_f32_32x32x16_f16 v[18:33], v[36:39], v[158:161], v[18:33]
	s_waitcnt lgkmcnt(0)
	v_mfma_f32_32x32x16_f16 v[2:17], v[40:43], v[158:161], v[2:17]
	s_nop 9
	v_max_f32_e32 v36, v19, v19
	v_max_f32_e32 v37, v18, v18
	v_max_f32_e32 v36, v37, v36
	v_max3_f32 v36, v36, v2, v4
	v_max3_f32 v37, v20, v21, v3
	v_max3_f32 v36, v36, v5, v22
	v_max3_f32 v37, v37, v24, v25
	v_max3_f32 v36, v36, v23, v6
	v_max3_f32 v37, v37, v8, v9
	v_max3_f32 v36, v36, v7, v26
	v_max3_f32 v37, v37, v28, v29
	v_max3_f32 v36, v36, v27, v10
	v_max3_f32 v37, v37, v12, v13
	v_max3_f32 v36, v36, v11, v30
	v_max3_f32 v37, v37, v32, v33
	v_max3_f32 v36, v36, v31, v14
	v_max3_f32 v37, v37, v16, v17
	v_max3_f32 v36, v36, v15, v37
	v_mov_b32_e32 v37, v36
	s_nop 1
	v_permlane32_swap_b32_e32 v36, v37
	v_max_f32_e32 v37, v37, v37
	v_max_f32_e32 v36, v36, v36
	v_max_f32_e32 v248, v36, v37
	v_sub_f32_e32 v39, v3, v248
	v_lshlrev_b32_e32 v3, 5, v0
	v_sub_f32_e32 v38, v2, v248
	v_and_b32_e32 v2, 32, v35
	v_and_b32_e32 v3, 0x180, v3
	v_lshlrev_b32_e32 v35, 3, v0
	v_sub_f32_e32 v40, v4, v248
	v_add3_u32 v3, s22, v229, v3
	v_and_b32_e32 v4, 24, v35
	v_add3_u32 v50, v3, v2, v4
	v_xor_b32_e32 v2, 0x80000000, v248
	v_sub_f32_e32 v41, v5, v248
	v_sub_f32_e32 v42, v6, v248
	v_sub_f32_e32 v43, v7, v248
	v_sub_f32_e32 v44, v8, v248
	v_sub_f32_e32 v45, v9, v248
	v_sub_f32_e32 v46, v10, v248
	v_sub_f32_e32 v47, v11, v248
	v_sub_f32_e32 v48, v12, v248
	v_sub_f32_e32 v49, v13, v248
	v_sub_f32_e32 v62, v14, v248
	v_sub_f32_e32 v63, v15, v248
	v_sub_f32_e32 v64, v16, v248
	v_sub_f32_e32 v65, v17, v248
	v_mov_b32_e32 v3, v2
	v_mov_b32_e32 v4, v2
	v_mov_b32_e32 v5, v2
	v_mov_b32_e32 v6, v2
	v_mov_b32_e32 v7, v2
	v_mov_b32_e32 v8, v2
	v_mov_b32_e32 v9, v2
	v_mov_b32_e32 v10, v2
	v_mov_b32_e32 v11, v2
	v_mov_b32_e32 v12, v2
	v_mov_b32_e32 v13, v2
	v_mov_b32_e32 v14, v2
	v_mov_b32_e32 v15, v2
	v_mov_b32_e32 v16, v2
	v_mov_b32_e32 v17, v2
	s_waitcnt vmcnt(0) lgkmcnt(0)
	s_barrier
	v_sub_f32_e32 v36, v18, v248
	v_sub_f32_e32 v37, v19, v248
	v_lshl_add_u64 v[18:19], s[20:21], 1, v[222:223]
	s_mov_b32 m0, s30
	s_nop 0
	global_load_lds_dwordx4 v[18:19], off
	v_lshl_add_u64 v[18:19], v[18:19], 0, s[10:11]
	s_mov_b32 m0, s19
	s_nop 0
	global_load_lds_dwordx4 v[18:19], off
	s_add_i32 s4, s31, 0x2000
	v_lshl_add_u64 v[18:19], v[224:225], 0, v[126:127]
	s_mov_b32 m0, s4
	s_nop 0
	global_load_lds_dwordx4 v[18:19], off
	v_lshl_add_u64 v[18:19], v[18:19], 0, s[10:11]
	s_add_i32 s4, s31, 0x3000
	s_mov_b32 m0, s4
	s_nop 0
	global_load_lds_dwordx4 v[18:19], off
	ds_read_b128 v[206:209], v234 offset:8192
	ds_read_b128 v[202:205], v234 offset:12288
	ds_read_b128 v[198:201], v235 offset:8192
	ds_read_b128 v[194:197], v235 offset:12288
	ds_read_b128 v[190:193], v236 offset:8192
	ds_read_b128 v[186:189], v236 offset:12288
	ds_read_b128 v[182:185], v237 offset:8192
	ds_read_b128 v[178:181], v237 offset:12288
	s_add_i32 s4, s1, 0x18c00
	s_add_i32 s18, s0, 0x18800
	v_sub_f32_e32 v20, v20, v248
	v_sub_f32_e32 v21, v21, v248
	v_sub_f32_e32 v22, v22, v248
	v_sub_f32_e32 v23, v23, v248
	v_sub_f32_e32 v24, v24, v248
	v_sub_f32_e32 v25, v25, v248
	v_sub_f32_e32 v26, v26, v248
	v_sub_f32_e32 v27, v27, v248
	v_sub_f32_e32 v28, v28, v248
	v_sub_f32_e32 v29, v29, v248
	v_sub_f32_e32 v30, v30, v248
	v_sub_f32_e32 v31, v31, v248
	v_sub_f32_e32 v32, v32, v248
	v_sub_f32_e32 v33, v33, v248
	v_and_b32_e32 v18, 64, v35
	s_add_u32 s8, s8, s2
	v_add_u32_e32 v240, v50, v18
	v_xad_u32 v239, v18, 64, v50
	v_exp_f32_e32 v66, v36
	v_exp_f32_e32 v67, v37
	v_exp_f32_e32 v50, v38
	v_exp_f32_e32 v51, v39
	v_exp_f32_e32 v68, v20
	v_exp_f32_e32 v52, v40
	v_exp_f32_e32 v69, v21
	v_exp_f32_e32 v53, v41
	v_exp_f32_e32 v70, v22
	v_exp_f32_e32 v54, v42
	v_exp_f32_e32 v71, v23
	v_exp_f32_e32 v55, v43
	v_exp_f32_e32 v72, v24
	v_exp_f32_e32 v56, v44
	v_exp_f32_e32 v73, v25
	v_exp_f32_e32 v57, v45
	v_exp_f32_e32 v74, v26
	v_exp_f32_e32 v58, v46
	v_exp_f32_e32 v75, v27
	v_exp_f32_e32 v59, v47
	v_exp_f32_e32 v76, v28
	v_exp_f32_e32 v60, v48
	v_exp_f32_e32 v77, v29
	v_exp_f32_e32 v61, v49
	v_exp_f32_e32 v78, v30
	v_exp_f32_e32 v62, v62
	v_exp_f32_e32 v79, v31
	v_exp_f32_e32 v63, v63
	v_exp_f32_e32 v80, v32
	v_exp_f32_e32 v64, v64
	v_exp_f32_e32 v81, v33
	v_exp_f32_e32 v65, v65
	s_addc_u32 s9, s9, s3
	s_lshl_b32 s17, s26, 1
	v_and_b32_e32 v0, 63, v0
	s_waitcnt vmcnt(4) lgkmcnt(0)
	s_barrier
	s_add_u32 s8, s8, s17
	v_mov_b32_e32 v35, v127
	v_cmp_gt_u32_e64 s[0:1], 32, v0
	s_addc_u32 s9, s9, 0
	v_lshl_add_u32 v232, v0, 2, s4
	v_lshlrev_b32_e32 v0, 2, v228
	v_add_u32_e32 v231, s24, v0
	v_add_u32_e32 v238, s18, v0
	v_lshl_add_u64 v[0:1], s[8:9], 0, v[34:35]
	s_sub_i32 s33, 0, s29
	v_mov_b32_e32 v34, v127
	v_mov_b32_e32 v36, v127
	v_mov_b32_e32 v37, v127
	v_mov_b32_e32 v38, v127
	v_mov_b32_e32 v39, v127
	v_mov_b32_e32 v40, v127
	v_mov_b32_e32 v41, v127
	v_mov_b32_e32 v42, v127
	v_mov_b32_e32 v43, v127
	v_mov_b32_e32 v44, v127
	v_mov_b32_e32 v45, v127
	v_mov_b32_e32 v46, v127
	v_mov_b32_e32 v47, v127
	v_mov_b32_e32 v48, v127
	v_mov_b32_e32 v49, v127
	v_mov_b32_e32 v18, v127
	v_mov_b32_e32 v19, v127
	v_mov_b32_e32 v20, v127
	v_mov_b32_e32 v21, v127
	v_mov_b32_e32 v22, v127
	v_mov_b32_e32 v23, v127
	v_mov_b32_e32 v24, v127
	v_mov_b32_e32 v25, v127
	v_mov_b32_e32 v26, v127
	v_mov_b32_e32 v27, v127
	v_mov_b32_e32 v28, v127
	v_mov_b32_e32 v29, v127
	v_mov_b32_e32 v30, v127
	v_mov_b32_e32 v31, v127
	v_mov_b32_e32 v32, v127
	v_mov_b32_e32 v33, v127
	s_branch .LBB1_2

.LBB1_6:
	s_waitcnt lgkmcnt(0)
	v_mfma_f32_32x32x16_f16 v[34:49], v[162:165], v[122:125], v[34:49]
	v_exp_f32_e32 v98, v98
	v_exp_f32_e32 v99, v99
	v_exp_f32_e32 v100, v100
	v_exp_f32_e32 v101, v101
	s_sub_i32 s43, s38, s27
	s_add_i32 s43, s43, 34
	s_add_i32 s44, s18, -1
	s_cmp_ge_i32 s44, s28
	s_cselect_b32 s45, s28, 0
	s_sub_i32 s44, s44, s45
	s_and_b64 s[48:49], s[6:7], exec
	s_cselect_b32 s43, s44, s43
	s_mul_i32 s54, s43, 0x22000
	v_lshl_add_u64 v[252:253], v[222:223], 0, s[54:55]
	s_add_i32 s44, s38, 1
	s_cmp_ge_i32 s44, s29
	s_cselect_b32 s44, s29, 0
	s_sub_i32 s44, 0, s44
	s_and_b64 s[48:49], s[6:7], exec
	s_cselect_b32 s44, s44, s28
	s_add_i32 s44, s44, s18
	s_add_i32 s44, s44, -3
	s_mul_i32 s56, s44, 0x22000
	v_lshl_add_u64 v[254:255], v[224:225], 0, s[56:57]
	s_add_i32 s52, s35, s30
	s_add_i32 s53, s36, s31
	v_mfma_f32_32x32x16_f16 v[18:33], v[162:165], v[118:121], v[18:33]
	v_exp_f32_e32 v102, v102
	v_exp_f32_e32 v103, v103
	v_exp_f32_e32 v104, v104
	v_exp_f32_e32 v105, v105
	v_add_u32_e32 v74, s36, v234
	ds_read_b128 v[62:65], v74
	ds_read_b128 v[138:141], v74 offset:4096
	v_mfma_f32_32x32x16_f16 v[34:49], v[166:169], v[114:117], v[34:49]
	v_exp_f32_e32 v106, v106
	v_exp_f32_e32 v107, v107
	v_exp_f32_e32 v108, v108
	v_exp_f32_e32 v109, v109
	v_add_u32_e32 v74, s36, v235
	ds_read_b128 v[178:181], v74
	ds_read_b128 v[126:129], v74 offset:4096
	v_mfma_f32_32x32x16_f16 v[18:33], v[166:169], v[70:73], v[18:33]
	v_exp_f32_e32 v110, v110
	v_exp_f32_e32 v111, v111
	v_exp_f32_e32 v112, v112
	v_exp_f32_e32 v113, v113
	v_add_u32_e32 v70, s36, v236
	ds_read_b128 v[130:133], v70
	ds_read_b128 v[118:121], v70 offset:4096
	v_mfma_f32_32x32x16_f16 v[34:49], v[170:173], v[66:69], v[34:49]
	v_exp_f32_e32 v82, v82
	v_exp_f32_e32 v83, v83
	v_exp_f32_e32 v84, v84
	v_exp_f32_e32 v85, v85
	v_add_u32_e32 v66, s36, v237
	ds_read_b128 v[122:125], v66
	ds_read_b128 v[114:117], v66 offset:4096
	v_mfma_f32_32x32x16_f16 v[18:33], v[170:173], v[50:53], v[18:33]
	v_exp_f32_e32 v86, v86
	v_exp_f32_e32 v87, v87
	v_exp_f32_e32 v88, v88
	v_exp_f32_e32 v89, v89
	v_mfma_f32_32x32x16_f16 v[34:49], v[174:177], v[54:57], v[34:49]
	v_exp_f32_e32 v90, v90
	v_exp_f32_e32 v91, v91
	v_exp_f32_e32 v92, v92
	v_exp_f32_e32 v93, v93
	v_mfma_f32_32x32x16_f16 v[18:33], v[174:177], v[58:61], v[18:33]
	v_exp_f32_e32 v94, v94
	v_exp_f32_e32 v95, v95
	v_exp_f32_e32 v96, v96
	v_exp_f32_e32 v97, v97
	s_mov_b32 m0, s52
	s_addk_i32 s52, 0x1000
	global_load_lds_dwordx4 v[252:253], off
	s_mov_b32 m0, s52
	v_lshl_add_u64 v[252:253], v[252:253], 0, s[10:11]
	global_load_lds_dwordx4 v[252:253], off
	s_mov_b32 m0, s53
	s_addk_i32 s53, 0x1000
	global_load_lds_dwordx4 v[254:255], off
	s_mov_b32 m0, s53
	v_lshl_add_u64 v[254:255], v[254:255], 0, s[10:11]
	global_load_lds_dwordx4 v[254:255], off
	s_waitcnt vmcnt(4) lgkmcnt(0)
	s_barrier
	s_andn2_b64 vcc, exec, s[8:9]
	s_cbranch_vccnz .LBB1_12
	v_add_u32_e32 v66, s24, v233
	ds_read_b128 v[50:53], v66 offset:96
	ds_read_b128 v[54:57], v66 offset:64
	ds_read_b128 v[58:61], v66 offset:32
	ds_read_b128 v[66:69], v66
	s_waitcnt lgkmcnt(3)
	v_pk_mul_f32 v[46:47], v[46:47], v[50:51]
	s_waitcnt lgkmcnt(2)
	v_pk_mul_f32 v[42:43], v[42:43], v[54:55]
	s_waitcnt lgkmcnt(1)
	v_pk_mul_f32 v[38:39], v[38:39], v[58:59]
	v_pk_mul_f32 v[48:49], v[48:49], v[52:53]
	v_pk_mul_f32 v[44:45], v[44:45], v[56:57]
	v_pk_mul_f32 v[40:41], v[40:41], v[60:61]
	s_waitcnt lgkmcnt(0)
	v_pk_mul_f32 v[36:37], v[36:37], v[68:69]
	v_pk_mul_f32 v[34:35], v[34:35], v[66:67]
	v_pk_mul_f32 v[30:31], v[30:31], v[50:51]
	v_pk_mul_f32 v[26:27], v[26:27], v[54:55]
	v_pk_mul_f32 v[22:23], v[22:23], v[58:59]
	v_pk_mul_f32 v[32:33], v[32:33], v[52:53]
	v_pk_mul_f32 v[28:29], v[28:29], v[56:57]
	v_pk_mul_f32 v[24:25], v[24:25], v[60:61]
	v_pk_mul_f32 v[20:21], v[20:21], v[68:69]
	v_pk_mul_f32 v[18:19], v[18:19], v[66:67]

.LBB1_13:
	s_add_i32 s16, s36, 0x2000
	s_cmpk_lg_i32 s36, 0x4000
	s_cselect_b32 s35, s16, 0
	s_waitcnt lgkmcnt(0)
	v_mfma_f32_32x32x16_f16 v[34:49], v[162:165], v[134:137], v[34:49]
	v_exp_f32_e32 v66, v66
	v_exp_f32_e32 v67, v67
	v_exp_f32_e32 v68, v68
	v_exp_f32_e32 v69, v69
	s_sub_i32 s43, s38, s27
	s_add_i32 s45, s43, 33
	s_add_i32 s43, s43, 35
	s_cmp_ge_i32 s18, s28
	s_cselect_b32 s44, s28, 0
	s_sub_i32 s44, s18, s44
	s_and_b64 s[48:49], s[6:7], exec
	s_cselect_b32 s43, s44, s43
	s_mul_i32 s54, s43, 0x22000
	v_lshl_add_u64 v[252:253], v[222:223], 0, s[54:55]
	s_add_i32 s44, s18, -2
	s_cmp_ge_i32 s44, s28
	s_cselect_b32 s46, s28, 0
	s_sub_i32 s44, s44, s46
	s_and_b64 s[48:49], s[6:7], exec
	s_cselect_b32 s44, s44, s45
	s_mul_i32 s56, s44, 0x22000
	v_lshl_add_u64 v[254:255], v[224:225], 0, s[56:57]
	s_add_i32 s52, s36, s30
	s_add_i32 s53, s35, s31
	s_add_i32 s46, s35, 0x2000
	s_cmpk_lg_i32 s35, 0x4000
	s_cselect_b32 s37, s46, 0
	s_add_i32 s39, s18, -2
	v_mfma_f32_32x32x16_f16 v[18:33], v[162:165], v[142:145], v[18:33]
	v_exp_f32_e32 v70, v70
	v_exp_f32_e32 v71, v71
	v_exp_f32_e32 v72, v72
	v_exp_f32_e32 v73, v73
	v_add_u32_e32 v94, s35, v234
	ds_read_b128 v[206:209], v94
	ds_read_b128 v[202:205], v94 offset:4096
	v_mfma_f32_32x32x16_f16 v[34:49], v[166:169], v[138:141], v[34:49]
	v_exp_f32_e32 v74, v74
	v_exp_f32_e32 v75, v75
	v_exp_f32_e32 v76, v76
	v_exp_f32_e32 v77, v77
	v_add_u32_e32 v94, s35, v235
	ds_read_b128 v[198:201], v94
	ds_read_b128 v[194:197], v94 offset:4096
	v_mfma_f32_32x32x16_f16 v[18:33], v[166:169], v[102:105], v[18:33]
	v_exp_f32_e32 v78, v78
	v_exp_f32_e32 v79, v79
	v_exp_f32_e32 v80, v80
	v_exp_f32_e32 v81, v81
	v_add_u32_e32 v94, s35, v236
	ds_read_b128 v[190:193], v94
	ds_read_b128 v[186:189], v94 offset:4096
	v_mfma_f32_32x32x16_f16 v[34:49], v[170:173], v[98:101], v[34:49]
	v_exp_f32_e32 v50, v50
	v_exp_f32_e32 v51, v51
	v_exp_f32_e32 v52, v52
	v_exp_f32_e32 v53, v53
	v_add_u32_e32 v94, s35, v237
	ds_read_b128 v[182:185], v94
	ds_read_b128 v[178:181], v94 offset:4096
	v_mfma_f32_32x32x16_f16 v[18:33], v[170:173], v[82:85], v[18:33]
	v_exp_f32_e32 v54, v54
	v_exp_f32_e32 v55, v55
	v_exp_f32_e32 v56, v56
	v_exp_f32_e32 v57, v57
	v_mfma_f32_32x32x16_f16 v[34:49], v[174:177], v[86:89], v[34:49]
	v_exp_f32_e32 v58, v58
	v_exp_f32_e32 v59, v59
	v_exp_f32_e32 v60, v60
	v_exp_f32_e32 v61, v61
	v_mfma_f32_32x32x16_f16 v[18:33], v[174:177], v[90:93], v[18:33]
	v_exp_f32_e32 v62, v62
	v_exp_f32_e32 v63, v63
	v_exp_f32_e32 v64, v64
	v_exp_f32_e32 v65, v65
	s_mov_b32 m0, s52
	s_addk_i32 s52, 0x1000
	global_load_lds_dwordx4 v[252:253], off
	s_mov_b32 m0, s52
	v_lshl_add_u64 v[252:253], v[252:253], 0, s[10:11]
	global_load_lds_dwordx4 v[252:253], off
	s_mov_b32 m0, s53
	s_addk_i32 s53, 0x1000
	global_load_lds_dwordx4 v[254:255], off
	s_mov_b32 m0, s53
	v_lshl_add_u64 v[254:255], v[254:255], 0, s[10:11]
	global_load_lds_dwordx4 v[254:255], off
	s_waitcnt vmcnt(4) lgkmcnt(0)
	s_barrier
	s_andn2_b64 vcc, exec, s[8:9]
	s_cbranch_vccnz .LBB1_23
	v_add_u32_e32 v94, s24, v233
	ds_read_b128 v[82:85], v94 offset:96
	ds_read_b128 v[86:89], v94 offset:64
	ds_read_b128 v[90:93], v94
	ds_read_b128 v[94:97], v94 offset:32
	s_waitcnt lgkmcnt(3)
	v_pk_mul_f32 v[48:49], v[48:49], v[84:85]
	v_pk_mul_f32 v[46:47], v[46:47], v[82:83]
	s_waitcnt lgkmcnt(2)
	v_pk_mul_f32 v[44:45], v[44:45], v[88:89]
	v_pk_mul_f32 v[42:43], v[42:43], v[86:87]
	s_waitcnt lgkmcnt(0)
	v_pk_mul_f32 v[40:41], v[40:41], v[96:97]
	v_pk_mul_f32 v[38:39], v[38:39], v[94:95]
	v_pk_mul_f32 v[36:37], v[36:37], v[92:93]
	v_pk_mul_f32 v[34:35], v[34:35], v[90:91]
	v_pk_mul_f32 v[32:33], v[32:33], v[84:85]
	v_pk_mul_f32 v[30:31], v[30:31], v[82:83]
	v_pk_mul_f32 v[28:29], v[28:29], v[88:89]
	v_pk_mul_f32 v[26:27], v[26:27], v[86:87]
	v_pk_mul_f32 v[24:25], v[24:25], v[96:97]
	v_pk_mul_f32 v[22:23], v[22:23], v[94:95]
	v_pk_mul_f32 v[20:21], v[20:21], v[92:93]
	v_pk_mul_f32 v[18:19], v[18:19], v[90:91]

	.amdhsa_kernel _Z10attn64_fwdPKDF16_S0_S0_PDF16_
		.amdhsa_group_segment_fixed_size 0
		.amdhsa_private_segment_fixed_size 0
		.amdhsa_kernarg_size 32
		.amdhsa_user_sgpr_count 2
		.amdhsa_user_sgpr_dispatch_ptr 0
		.amdhsa_user_sgpr_queue_ptr 0
		.amdhsa_user_sgpr_kernarg_segment_ptr 1
		.amdhsa_user_sgpr_dispatch_id 0
		.amdhsa_user_sgpr_kernarg_preload_length 0
		.amdhsa_user_sgpr_kernarg_preload_offset 0
		.amdhsa_user_sgpr_private_segment_size 0
		.amdhsa_uses_dynamic_stack 0
		.amdhsa_enable_private_segment 0
		.amdhsa_system_sgpr_workgroup_id_x 1
		.amdhsa_system_sgpr_workgroup_id_y 0
		.amdhsa_system_sgpr_workgroup_id_z 0
		.amdhsa_system_sgpr_workgroup_info 0
		.amdhsa_system_vgpr_workitem_id 0
		.amdhsa_next_free_vgpr 256
		.amdhsa_next_free_sgpr 58
		.amdhsa_accum_offset 256
		.amdhsa_reserve_vcc 1
		.amdhsa_float_round_mode_32 0
		.amdhsa_float_round_mode_16_64 0
		.amdhsa_float_denorm_mode_32 3
		.amdhsa_float_denorm_mode_16_64 3
		.amdhsa_dx10_clamp 1
		.amdhsa_ieee_mode 1
		.amdhsa_fp16_overflow 0
		.amdhsa_tg_split 0
		.amdhsa_exception_fp_ieee_invalid_op 0
		.amdhsa_exception_fp_denorm_src 0
		.amdhsa_exception_fp_ieee_div_zero 0
		.amdhsa_exception_fp_ieee_overflow 0
		.amdhsa_exception_fp_ieee_underflow 0
		.amdhsa_exception_fp_ieee_inexact 0
		.amdhsa_exception_int_div_zero 0
	.end_amdhsa_kernel

amdhsa.kernels:
  - .agpr_count:     0
    .args:
      - .actual_access:  read_only
        .address_space:  global
        .offset:         0
        .size:           8
        .value_kind:     global_buffer
      - .actual_access:  read_only
        .address_space:  global
        .offset:         8
        .size:           8
        .value_kind:     global_buffer
      - .actual_access:  read_only
        .address_space:  global
        .offset:         16
        .size:           8
        .value_kind:     global_buffer
      - .actual_access:  read_only
        .address_space:  global
        .offset:         24
        .size:           8
        .value_kind:     global_buffer
      - .actual_access:  read_only
        .address_space:  global
        .offset:         32
        .size:           8
        .value_kind:     global_buffer
      - .address_space:  global
        .offset:         40
        .size:           8
        .value_kind:     global_buffer
      - .address_space:  global
        .offset:         48
        .size:           8
        .value_kind:     global_buffer
      - .address_space:  global
        .offset:         56
        .size:           8
        .value_kind:     global_buffer
      - .address_space:  global
        .offset:         64
        .size:           8
        .value_kind:     global_buffer
    .group_segment_fixed_size: 0
    .kernarg_segment_align: 8
    .kernarg_segment_size: 72
    .language:       OpenCL C
    .language_version:
      - 2
      - 0
    .max_flat_workgroup_size: 256
    .name:           _Z11prep_kernelPKfS0_S0_S0_S0_PDF16_S1_S1_P15HIP_vector_typeIfLj2EE
    .private_segment_fixed_size: 0
    .sgpr_count:     32
    .sgpr_spill_count: 0
    .symbol:         _Z11prep_kernelPKfS0_S0_S0_S0_PDF16_S1_S1_P15HIP_vector_typeIfLj2EE.kd
    .uniform_work_group_size: 1
    .uses_dynamic_stack: false
    .vgpr_count:     20
    .vgpr_spill_count: 0
    .wavefront_size: 64
  - .agpr_count:     0
    .args:
      - .address_space:  global
        .offset:         0
        .size:           8
        .value_kind:     global_buffer
      - .address_space:  global
        .offset:         8
        .size:           8
        .value_kind:     global_buffer
      - .address_space:  global
        .offset:         16
        .size:           8
        .value_kind:     global_buffer
      - .address_space:  global
        .offset:         24
        .size:           8
        .value_kind:     global_buffer
    .group_segment_fixed_size: 0
    .kernarg_segment_align: 8
    .kernarg_segment_size: 32
    .language:       OpenCL C
    .language_version:
      - 2
      - 0
    .max_flat_workgroup_size: 512
    .name:           _Z10attn64_fwdPKDF16_S0_S0_PDF16_
    .private_segment_fixed_size: 0
    .sgpr_count:     64
    .sgpr_spill_count: 0
    .symbol:         _Z10attn64_fwdPKDF16_S0_S0_PDF16_.kd
    .uniform_work_group_size: 1
    .uses_dynamic_stack: false
    .vgpr_count:     256
    .vgpr_spill_count: 0
    .wavefront_size: 64
  - .agpr_count:     0
    .args:
      - .address_space:  global
        .offset:         0
        .size:           8
        .value_kind:     global_buffer
      - .address_space:  global
        .offset:         8
        .size:           8
        .value_kind:     global_buffer
      - .address_space:  global
        .offset:         16
        .size:           8
        .value_kind:     global_buffer
      - .address_space:  global
        .offset:         24
        .size:           8
        .value_kind:     global_buffer
      - .address_space:  global
        .offset:         32
        .size:           8
        .value_kind:     global_buffer
      - .address_space:  global
        .offset:         40
        .size:           8
        .value_kind:     global_buffer
      - .actual_access:  read_only
        .address_space:  global
        .offset:         48
        .size:           8
        .value_kind:     global_buffer
      - .offset:         56
        .size:           4
        .value_kind:     by_value
      - .offset:         60
        .size:           4
        .value_kind:     by_value
      - .offset:         64
        .size:           4
        .value_kind:     by_value
    .group_segment_fixed_size: 32768
    .kernarg_segment_align: 8
    .kernarg_segment_size: 68
    .language:       OpenCL C
    .language_version:
      - 2
      - 0
    .max_flat_workgroup_size: 768
    .name:           _Z7gemm_dbILi256ELi192ELi64ELi96ELi64ELi2ELi1ELi4EEvPKDF16_S1_PfPDF16_S3_S3_PK15HIP_vector_typeIfLj2EEiii
    .private_segment_fixed_size: 0
    .sgpr_count:     27
    .sgpr_spill_count: 0
    .symbol:         _Z7gemm_dbILi256ELi192ELi64ELi96ELi64ELi2ELi1ELi4EEvPKDF16_S1_PfPDF16_S3_S3_PK15HIP_vector_typeIfLj2EEiii.kd
    .uniform_work_group_size: 1
    .uses_dynamic_stack: false
    .vgpr_count:     141
    .vgpr_spill_count: 0
    .wavefront_size: 64
  - .agpr_count:     0
    .args:
      - .address_space:  global
        .offset:         0
        .size:           8
        .value_kind:     global_buffer
      - .address_space:  global
        .offset:         8
        .size:           8
        .value_kind:     global_buffer
      - .address_space:  global
        .offset:         16
        .size:           8
        .value_kind:     global_buffer
      - .address_space:  global
        .offset:         24
        .size:           8
        .value_kind:     global_buffer
      - .address_space:  global
        .offset:         32
        .size:           8
        .value_kind:     global_buffer
      - .address_space:  global
        .offset:         40
        .size:           8
        .value_kind:     global_buffer
      - .actual_access:  read_only
        .address_space:  global
        .offset:         48
        .size:           8
        .value_kind:     global_buffer
      - .offset:         56
        .size:           4
        .value_kind:     by_value
      - .offset:         60
        .size:           4
        .value_kind:     by_value
      - .offset:         64
        .size:           4
        .value_kind:     by_value
    .group_segment_fixed_size: 0
    .kernarg_segment_align: 8
    .kernarg_segment_size: 68
    .language:       OpenCL C
    .language_version:
      - 2
      - 0
    .max_flat_workgroup_size: 512
    .name:           _Z7gemm_dbILi128ELi128ELi64ELi64ELi64ELi3ELi0ELi4EEvPKDF16_S1_PfPDF16_S3_S3_PK15HIP_vector_typeIfLj2EEiii
    .private_segment_fixed_size: 0
    .sgpr_count:     26
    .sgpr_spill_count: 0
    .symbol:         _Z7gemm_dbILi128ELi128ELi64ELi64ELi64ELi3ELi0ELi4EEvPKDF16_S1_PfPDF16_S3_S3_PK15HIP_vector_typeIfLj2EEiii.kd
    .uniform_work_group_size: 1
    .uses_dynamic_stack: false
    .vgpr_count:     168
    .vgpr_spill_count: 0
    .wavefront_size: 64
